# speedup vs baseline: 1.0280x; 1.0280x over previous
_Z7k_attn3PKDF16_S0_PKiS2_PiPKDv8_DF16_PKfS6_S8_Pf:
	s_load_dwordx2 s[12:13], s[0:1], 0x8
	s_load_dwordx2 s[4:5], s[0:1], 0x18
	s_load_dwordx2 s[6:7], s[0:1], 0x28
	s_load_dwordx2 s[16:17], s[0:1], 0x10
	v_lshlrev_b32_e32 v13, 4, v0
	s_mul_i32 s3, s2, 0xc350
	v_or_b32_e32 v1, 0x4000, v13
	s_add_i32 s8, s3, 0xc350
	s_lshl_b32 s20, s2, 2
	s_waitcnt lgkmcnt(0)
	s_add_u32 s4, s4, s20
	s_addc_u32 s5, s5, 0
	s_load_dwordx2 s[18:19], s[4:5], 0x0
	global_load_dwordx4 v[100:103], v13, s[6:7]
	global_load_dwordx4 v[104:107], v1, s[6:7]
	v_or_b32_e32 v1, 0x8000, v13
	s_ashr_i32 s9, s8, 31
	v_or_b32_e32 v2, 0xc000, v13
	global_load_dwordx4 v[108:111], v1, s[6:7]
	global_load_dwordx4 v[112:115], v2, s[6:7]
	v_mov_b32_e32 v116, v13
	s_ashr_i32 s6, s3, 31
	s_lshr_b32 s9, s9, 24
	s_lshr_b32 s6, s6, 24
	s_add_i32 s8, s8, s9
	s_add_i32 s3, s3, s6
	v_lshrrev_b32_e32 v80, 6, v0
	s_ashr_i32 s8, s8, 8
	s_ashr_i32 s66, s3, 8
	s_sub_i32 s33, s8, s66
	v_lshlrev_b32_e32 v1, 1, v80
	v_and_b32_e32 v79, 15, v0
	s_add_i32 s67, s33, -1
	v_or_b32_e32 v11, 1, v1
	v_min_i32_e32 v12, s67, v1
	v_min_i32_e32 v10, s67, v11
	v_cmp_gt_u32_e64 s[38:39], 8, v79
	v_bfe_u32 v28, v0, 4, 2
	v_cmp_eq_u32_e32 vcc, 0, v0
	v_cndmask_b32_e64 v1, v10, v12, s[38:39]
	v_add_u32_e32 v2, s66, v1
	v_ashrrev_i32_e32 v3, 31, v2
	v_lshlrev_b64 v[2:3], 8, v[2:3]
	v_and_b32_e32 v1, 0x70, v13
	v_lshl_add_u64 v[8:9], s[12:13], 0, v[2:3]
	v_lshlrev_b32_e32 v2, 1, v1
	v_lshlrev_b32_e32 v1, 3, v28
	v_mov_b32_e32 v3, 0
	v_and_b32_e32 v22, 8, v1
	v_lshl_add_u64 v[8:9], v[8:9], 0, v[2:3]
	v_lshlrev_b32_e32 v26, 1, v22
	v_mov_b32_e32 v27, v3
	v_lshl_add_u64 v[8:9], v[8:9], 0, v[26:27]
	global_load_dwordx4 v[22:25], v[8:9], off nt
	s_and_saveexec_b64 s[6:7], vcc
	v_mov_b32_e32 v3, 16
	v_mov_b32_e32 v4, 0x26b40
	ds_write_b32 v4, v3
	s_or_b64 exec, exec, s[6:7]
	v_cmp_gt_u32_e32 vcc, 32, v0
	s_and_saveexec_b64 s[6:7], vcc
	v_mov_b32_e32 v3, 0x26d50
	v_lshl_add_u32 v3, v0, 2, v3
	v_mov_b32_e32 v4, 0
	ds_write_b32 v3, v4
	s_or_b64 exec, exec, s[6:7]
	s_movk_i32 s3, 0x100
	v_cmp_gt_u32_e32 vcc, s3, v0
	s_and_saveexec_b64 s[4:5], vcc
	v_mov_b32_e32 v3, 0x1dd00
	v_lshl_add_u32 v3, v0, 2, v3
	v_mov_b32_e32 v4, 0
	ds_write2st64_b32 v3, v4, v4 offset1:4
	s_or_b64 exec, exec, s[4:5]
	s_waitcnt lgkmcnt(0)
	s_cmp_gt_i32 s19, s18
	s_cselect_b64 s[6:7], -1, 0
	s_add_i32 s24, s19, -1
	s_cmp_le_i32 s19, s18
	v_add_u32_e32 v3, s18, v0
	v_mov_b32_e32 v13, 0
	v_mov_b32_e32 v15, 0
	s_barrier
	s_cbranch_scc0 .LBB0_50
	v_cndmask_b32_e64 v4, 0, 1, s[6:7]
	v_cmp_ne_u32_e64 s[4:5], 1, v4
	s_andn2_b64 vcc, exec, s[6:7]
	s_cbranch_vccz .LBB0_51

.LBB0_105:
	s_or_b64 exec, exec, s[0:1]
	s_lshr_b32 s95, s80, 3
	s_lshl_b32 s95, s95, 2
	s_add_i32 s95, s95, 0x26d60
	v_mov_b32_e32 v2, s95
	v_mov_b32_e32 v4, 1
	s_mov_b64 exec, 1
	ds_add_u32 v2, v4
	s_mov_b64 exec, -1
	s_and_saveexec_b64 s[0:1], s[78:79]
	s_cbranch_execz .LBB0_107
	ds_read_b128 v[4:7], v86
	ds_read_b128 v[8:11], v86 offset:1024
	ds_read_b128 v[12:15], v86 offset:4096
	ds_read_b128 v[22:25], v86 offset:5120
	ds_read_b128 v[34:37], v86 offset:2048
	ds_read_b128 v[38:41], v86 offset:3072
	ds_read_b128 v[42:45], v86 offset:6144
	ds_read_b128 v[46:49], v86 offset:7168
	v_cndmask_b32_e64 v21, 0, v102, s[22:23]
	v_cndmask_b32_e64 v20, 0, v101, s[22:23]
	v_cndmask_b32_e64 v19, 0, v100, s[22:23]
	v_cndmask_b32_e64 v18, 0, v99, s[22:23]
	v_cndmask_b32_e64 v29, 0, v102, s[24:25]
	v_cndmask_b32_e64 v28, 0, v101, s[24:25]
	v_cndmask_b32_e64 v27, 0, v100, s[24:25]
	v_cndmask_b32_e64 v26, 0, v99, s[24:25]
	v_cndmask_b32_e64 v33, 0, v102, s[26:27]
	v_cndmask_b32_e64 v32, 0, v101, s[26:27]
	v_cndmask_b32_e64 v31, 0, v100, s[26:27]
	v_cndmask_b32_e64 v30, 0, v99, s[26:27]
	v_cndmask_b32_e64 v53, 0, v102, s[28:29]
	v_cndmask_b32_e64 v52, 0, v101, s[28:29]
	v_cndmask_b32_e64 v51, 0, v100, s[28:29]
	v_cndmask_b32_e64 v50, 0, v99, s[28:29]
	s_waitcnt lgkmcnt(7)
	v_mfma_f32_16x16x32_f16 v[4:7], v[4:7], v[18:21], 0
	s_waitcnt lgkmcnt(5)
	v_mfma_f32_16x16x32_f16 v[12:15], v[12:15], v[18:21], 0
	v_mfma_f32_16x16x32_f16 v[4:7], v[8:11], v[26:29], v[4:7]
	s_waitcnt lgkmcnt(4)
	v_mfma_f32_16x16x32_f16 v[8:11], v[22:25], v[26:29], v[12:15]
	s_nop 4
	ds_read_b128 v[12:15], v86 offset:13312
	ds_read_b128 v[22:25], v86 offset:12288
	ds_read_b128 v[54:57], v86 offset:9216
	ds_read_b128 v[58:61], v86 offset:8192
	s_waitcnt lgkmcnt(7)
	v_mfma_f32_16x16x32_f16 v[4:7], v[34:37], v[30:33], v[4:7]
	s_waitcnt lgkmcnt(5)
	v_mfma_f32_16x16x32_f16 v[8:11], v[42:45], v[30:33], v[8:11]
	s_waitcnt lgkmcnt(4)
	v_mfma_f32_16x16x32_f16 v[34:37], v[46:49], v[50:53], v[8:11]
	v_mfma_f32_16x16x32_f16 v[4:7], v[38:41], v[50:53], v[4:7]
	s_nop 6
	v_cvt_pk_f16_f32 v9, v36, v37
	v_cvt_pk_f16_f32 v8, v34, v35
	v_cvt_pk_f16_f32 v7, v6, v7
	v_cvt_pk_f16_f32 v6, v4, v5
	ds_read_b128 v[34:37], v86 offset:10240
	ds_read_b128 v[38:41], v86 offset:11264
	ds_read_b128 v[42:45], v86 offset:14336
	ds_read_b128 v[46:49], v86 offset:15360
	s_waitcnt lgkmcnt(6)
	v_mfma_f32_16x16x32_f16 v[22:25], v[22:25], v[18:21], 0
	s_waitcnt lgkmcnt(4)
	v_mfma_f32_16x16x32_f16 v[58:61], v[58:61], v[18:21], 0
	v_mfma_f32_16x16x32_f16 v[10:13], v[12:15], v[26:29], v[22:25]
	v_mfma_f32_16x16x32_f16 v[54:57], v[54:57], v[26:29], v[58:61]
	ds_read_b128 v[14:17], v86 offset:21504
	s_nop 2
	ds_read_b128 v[22:25], v86 offset:20480
	s_nop 0
	ds_read_b128 v[58:61], v86 offset:17408
	ds_read_b128 v[62:65], v86 offset:16384
	s_waitcnt lgkmcnt(7)
	v_mfma_f32_16x16x32_f16 v[34:37], v[34:37], v[30:33], v[54:57]
	s_waitcnt lgkmcnt(5)
	v_mfma_f32_16x16x32_f16 v[10:13], v[42:45], v[30:33], v[10:13]
	s_waitcnt lgkmcnt(4)
	v_mfma_f32_16x16x32_f16 v[10:13], v[46:49], v[50:53], v[10:13]
	v_mfma_f32_16x16x32_f16 v[34:37], v[38:41], v[50:53], v[34:37]
	s_nop 6
	v_cvt_pk_f16_f32 v13, v12, v13
	v_cvt_pk_f16_f32 v12, v10, v11
	v_cvt_pk_f16_f32 v11, v36, v37
	v_cvt_pk_f16_f32 v10, v34, v35
	ds_read_b128 v[34:37], v86 offset:18432
	ds_read_b128 v[38:41], v86 offset:19456
	ds_read_b128 v[42:45], v86 offset:22528
	ds_read_b128 v[46:49], v86 offset:23552
	s_waitcnt lgkmcnt(6)
	v_mfma_f32_16x16x32_f16 v[22:25], v[22:25], v[18:21], 0
	s_waitcnt lgkmcnt(4)
	v_mfma_f32_16x16x32_f16 v[54:57], v[62:65], v[18:21], 0
	v_mfma_f32_16x16x32_f16 v[14:17], v[14:17], v[26:29], v[22:25]
	v_mfma_f32_16x16x32_f16 v[54:57], v[58:61], v[26:29], v[54:57]
	s_nop 3
	ds_read_b128 v[22:25], v86 offset:29696
	ds_read_b128 v[58:61], v86 offset:28672
	ds_read_b128 v[62:65], v86 offset:25600
	ds_read_b128 v[66:69], v86 offset:24576
	s_waitcnt lgkmcnt(7)
	v_mfma_f32_16x16x32_f16 v[34:37], v[34:37], v[30:33], v[54:57]
	s_waitcnt lgkmcnt(5)
	v_mfma_f32_16x16x32_f16 v[14:17], v[42:45], v[30:33], v[14:17]
	s_waitcnt lgkmcnt(4)
	v_mfma_f32_16x16x32_f16 v[14:17], v[46:49], v[50:53], v[14:17]
	v_mfma_f32_16x16x32_f16 v[34:37], v[38:41], v[50:53], v[34:37]
	s_nop 6
	v_cvt_pk_f16_f32 v17, v16, v17
	v_cvt_pk_f16_f32 v16, v14, v15
	v_cvt_pk_f16_f32 v15, v36, v37
	v_cvt_pk_f16_f32 v14, v34, v35
	ds_read_b128 v[34:37], v86 offset:26624
	ds_read_b128 v[38:41], v86 offset:27648
	ds_read_b128 v[42:45], v86 offset:30720
	ds_read_b128 v[46:49], v86 offset:31744
	s_waitcnt lgkmcnt(4)
	v_mfma_f32_16x16x32_f16 v[54:57], v[66:69], v[18:21], 0
	v_mfma_f32_16x16x32_f16 v[18:21], v[58:61], v[18:21], 0
	v_mfma_f32_16x16x32_f16 v[18:21], v[22:25], v[26:29], v[18:21]
	v_mfma_f32_16x16x32_f16 v[54:57], v[62:65], v[26:29], v[54:57]
	s_waitcnt lgkmcnt(3)
	v_mfma_f32_16x16x32_f16 v[22:25], v[34:37], v[30:33], v[54:57]
	s_waitcnt lgkmcnt(1)
	v_mfma_f32_16x16x32_f16 v[18:21], v[42:45], v[30:33], v[18:21]
	s_waitcnt lgkmcnt(0)
	v_mfma_f32_16x16x32_f16 v[18:21], v[46:49], v[50:53], v[18:21]
	v_mfma_f32_16x16x32_f16 v[22:25], v[38:41], v[50:53], v[22:25]
	s_nop 6
	v_cvt_pk_f16_f32 v21, v20, v21
	v_cvt_pk_f16_f32 v20, v18, v19
	v_cvt_pk_f16_f32 v19, v24, v25
	v_cvt_pk_f16_f32 v18, v22, v23

.LBB0_118:
	s_or_b64 exec, exec, s[60:61]
	v_readfirstlane_b32 s74, v0
	v_mov_b32_e32 v42, 0
	v_mov_b32_e32 v50, 0
	v_bfe_u32 v36, v0, 6, 2
	v_lshl_or_b32 v44, v36, 13, v86
	v_mov_b32_e32 v45, 0
	v_lshl_add_u64 v[18:19], s[56:57], 0, v[44:45]
	v_add_co_u32_e32 v34, vcc, 0x1000, v18
	global_load_dwordx4 v[2:5], v44, s[56:57]
	global_load_dwordx4 v[6:9], v44, s[56:57] offset:1024
	global_load_dwordx4 v[10:13], v44, s[56:57] offset:2048
	global_load_dwordx4 v[14:17], v44, s[56:57] offset:3072
	v_addc_co_u32_e32 v35, vcc, 0, v19, vcc
	v_lshlrev_b32_e32 v44, 7, v36
	global_load_dwordx4 v[18:21], v[34:35], off
	global_load_dwordx4 v[22:25], v[34:35], off offset:1024
	global_load_dwordx4 v[26:29], v[34:35], off offset:2048
	global_load_dwordx4 v[30:33], v[34:35], off offset:3072
	v_lshl_add_u64 v[34:35], s[52:53], 0, v[44:45]
	v_lshlrev_b32_e32 v36, 2, v1
	v_mov_b32_e32 v37, v45
	v_lshl_add_u64 v[46:47], v[34:35], 0, v[36:37]
	global_load_dwordx4 v[34:37], v[46:47], off offset:16
	global_load_dwordx4 v[38:41], v[46:47], off
	v_add3_u32 v46, s66, v50, v79
	v_ashrrev_i32_e32 v47, 31, v46
	v_and_b32_e32 v0, 48, v0
	v_lshlrev_b64 v[46:47], 9, v[46:47]
	v_lshlrev_b32_e32 v0, 1, v0
	v_or3_b32 v46, v46, v44, v0
	v_mul_u32_u24_e32 v43, 0x110, v79
	s_movk_i32 s0, 0x1100
	v_lshl_add_u64 v[0:1], s[54:55], 0, v[46:47]
	v_mad_u32_u24 v42, v42, s0, v43
	s_mov_b32 s0, 0x10000
	v_lshl_add_u64 v[0:1], v[0:1], 0, 16
	v_add3_u32 v51, v42, v70, s0
	s_lshr_b32 s74, s74, 6
	s_and_b32 s74, s74, 3
	s_lshl_b32 s75, s74, 2
	s_add_i32 s75, s75, 0x26d50
	s_add_i32 s76, s33, 15
	s_lshr_b32 s76, s76, 4
	v_mov_b64_e32 v[60:61], v[0:1]
	v_mov_b32_e32 v62, v51
	s_waitcnt vmcnt(0)
.Lep_claim:
	v_mov_b32_e32 v63, s75
	v_mov_b32_e32 v64, 1
	s_mov_b64 exec, 1
	ds_add_rtn_u32 v64, v63, v64
	s_mov_b64 exec, -1
	s_waitcnt lgkmcnt(0)
	v_readfirstlane_b32 s77, v64
	s_cmp_ge_i32 s77, s76
	s_cbranch_scc1 .LBB0_123
	s_lshl_b32 s94, s77, 3
	s_sub_i32 s94, s68, s94
	s_min_i32 s94, s94, 8
	s_lshl_b32 s95, s77, 2
	s_add_i32 s95, s95, 0x26d60
	v_mov_b32_e32 v63, s95
	s_mov_b32 s73, 0
.Lep_wait:
	ds_read_b32 v64, v63
	s_waitcnt lgkmcnt(0)
	v_readfirstlane_b32 s95, v64
	s_cmp_ge_i32 s95, s94
	s_cbranch_scc1 .Lep_go
	s_sleep 4
	s_add_i32 s73, s73, 1
	s_cmp_lt_u32 s73, 0x40000
	s_cbranch_scc1 .Lep_wait
.Lep_go:
	s_lshl_b32 s95, s77, 4
	v_mov_b32_e32 v50, s95
	s_mul_i32 s95, s77, 0x1100
	v_add_u32_e32 v51, s95, v62
	s_lshl_b32 s94, s77, 13
	s_mov_b32 s95, 0
	v_lshl_add_u64 v[0:1], v[60:61], 0, s[94:95]
	ds_read_b128 v[42:45], v51
	ds_read_b128 v[46:49], v51 offset:64
	s_waitcnt lgkmcnt(1)
	v_mfma_f32_16x16x32_f16 v[52:55], v[2:5], v[42:45], v[38:41]
	v_mfma_f32_16x16x32_f16 v[42:45], v[18:21], v[42:45], v[34:37]
	s_waitcnt lgkmcnt(0)
	v_mfma_f32_16x16x32_f16 v[52:55], v[6:9], v[46:49], v[52:55]
	v_mfma_f32_16x16x32_f16 v[42:45], v[22:25], v[46:49], v[42:45]
	ds_read_b128 v[46:49], v51 offset:128
	ds_read_b128 v[56:59], v51 offset:192
	s_waitcnt lgkmcnt(1)
	v_mfma_f32_16x16x32_f16 v[52:55], v[10:13], v[46:49], v[52:55]
	v_mfma_f32_16x16x32_f16 v[46:49], v[26:29], v[46:49], v[42:45]
	s_waitcnt lgkmcnt(0)
	v_mfma_f32_16x16x32_f16 v[42:45], v[14:17], v[56:59], v[52:55]
	v_mfma_f32_16x16x32_f16 v[46:49], v[30:33], v[56:59], v[46:49]
	s_nop 3
	v_add_u32_e32 v52, v79, v50
	v_cmp_gt_i32_e32 vcc, s33, v52
	s_and_saveexec_b64 s[4:5], vcc
	s_cbranch_execz .Lep_next
	global_store_dwordx4 v[0:1], v[42:45], off offset:-16 nt
	global_store_dwordx4 v[0:1], v[46:49], off nt
.Lep_next:
	s_or_b64 exec, exec, s[4:5]
	s_branch .Lep_claim

	.amdhsa_kernel _Z7k_attn3PKDF16_S0_PKiS2_PiPKDv8_DF16_PKfS6_S8_Pf
		.amdhsa_group_segment_fixed_size 159184
		.amdhsa_private_segment_fixed_size 0
		.amdhsa_kernarg_size 80
		.amdhsa_user_sgpr_count 2
		.amdhsa_user_sgpr_dispatch_ptr 0
		.amdhsa_user_sgpr_queue_ptr 0
		.amdhsa_user_sgpr_kernarg_segment_ptr 1
		.amdhsa_user_sgpr_dispatch_id 0
		.amdhsa_user_sgpr_kernarg_preload_length 0
		.amdhsa_user_sgpr_kernarg_preload_offset 0
		.amdhsa_user_sgpr_private_segment_size 0
		.amdhsa_uses_dynamic_stack 0
		.amdhsa_enable_private_segment 0
		.amdhsa_system_sgpr_workgroup_id_x 1
		.amdhsa_system_sgpr_workgroup_id_y 0
		.amdhsa_system_sgpr_workgroup_id_z 0
		.amdhsa_system_sgpr_workgroup_info 0
		.amdhsa_system_vgpr_workitem_id 0
		.amdhsa_next_free_vgpr 128
		.amdhsa_next_free_sgpr 102
		.amdhsa_accum_offset 128
		.amdhsa_reserve_vcc 1
		.amdhsa_float_round_mode_32 0
		.amdhsa_float_round_mode_16_64 0
		.amdhsa_float_denorm_mode_32 3
		.amdhsa_float_denorm_mode_16_64 3
		.amdhsa_dx10_clamp 1
		.amdhsa_ieee_mode 1
		.amdhsa_fp16_overflow 0
		.amdhsa_tg_split 0
		.amdhsa_exception_fp_ieee_invalid_op 0
		.amdhsa_exception_fp_denorm_src 0
		.amdhsa_exception_fp_ieee_div_zero 0
		.amdhsa_exception_fp_ieee_overflow 0
		.amdhsa_exception_fp_ieee_underflow 0
		.amdhsa_exception_fp_ieee_inexact 0
		.amdhsa_exception_int_div_zero 0
	.end_amdhsa_kernel

amdhsa.kernels:
  - .agpr_count:     0
    .args:
      - .actual_access:  read_only
        .address_space:  global
        .offset:         0
        .size:           8
        .value_kind:     global_buffer
      - .actual_access:  read_only
        .address_space:  global
        .offset:         8
        .size:           8
        .value_kind:     global_buffer
      - .actual_access:  read_only
        .address_space:  global
        .offset:         16
        .size:           8
        .value_kind:     global_buffer
      - .actual_access:  read_only
        .address_space:  global
        .offset:         24
        .size:           8
        .value_kind:     global_buffer
      - .address_space:  global
        .offset:         32
        .size:           8
        .value_kind:     global_buffer
      - .actual_access:  read_only
        .address_space:  global
        .offset:         40
        .size:           8
        .value_kind:     global_buffer
      - .actual_access:  read_only
        .address_space:  global
        .offset:         48
        .size:           8
        .value_kind:     global_buffer
      - .actual_access:  read_only
        .address_space:  global
        .offset:         56
        .size:           8
        .value_kind:     global_buffer
      - .actual_access:  read_only
        .address_space:  global
        .offset:         64
        .size:           8
        .value_kind:     global_buffer
      - .actual_access:  write_only
        .address_space:  global
        .offset:         72
        .size:           8
        .value_kind:     global_buffer
    .group_segment_fixed_size: 159184
    .kernarg_segment_align: 8
    .kernarg_segment_size: 80
    .language:       OpenCL C
    .language_version:
      - 2
      - 0
    .max_flat_workgroup_size: 1024
    .name:           _Z7k_attn3PKDF16_S0_PKiS2_PiPKDv8_DF16_PKfS6_S8_Pf
    .private_segment_fixed_size: 0
    .sgpr_count:     79
    .sgpr_spill_count: 0
    .symbol:         _Z7k_attn3PKDF16_S0_PKiS2_PiPKDv8_DF16_PKfS6_S8_Pf.kd
    .uniform_work_group_size: 1
    .uses_dynamic_stack: false
    .vgpr_count:     128
    .vgpr_spill_count: 0
    .wavefront_size: 64
  - .agpr_count:     0
    .args:
      - .actual_access:  read_only
        .address_space:  global
        .offset:         0
        .size:           8
        .value_kind:     global_buffer
      - .actual_access:  write_only
        .address_space:  global
        .offset:         8
        .size:           8
        .value_kind:     global_buffer
      - .actual_access:  read_only
        .address_space:  global
        .offset:         16
        .size:           8
        .value_kind:     global_buffer
      - .actual_access:  read_only
        .address_space:  global
        .offset:         24
        .size:           8
        .value_kind:     global_buffer
      - .actual_access:  read_only
        .address_space:  global
        .offset:         32
        .size:           8
        .value_kind:     global_buffer
      - .actual_access:  read_only
        .address_space:  global
        .offset:         40
        .size:           8
        .value_kind:     global_buffer
      - .actual_access:  read_only
        .address_space:  global
        .offset:         48
        .size:           8
        .value_kind:     global_buffer
      - .actual_access:  read_only
        .address_space:  global
        .offset:         56
        .size:           8
        .value_kind:     global_buffer
      - .actual_access:  read_only
        .address_space:  global
        .offset:         64
        .size:           8
        .value_kind:     global_buffer
      - .actual_access:  write_only
        .address_space:  global
        .offset:         72
        .size:           8
        .value_kind:     global_buffer
      - .actual_access:  write_only
        .address_space:  global
        .offset:         80
        .size:           8
        .value_kind:     global_buffer
      - .actual_access:  write_only
        .address_space:  global
        .offset:         88
        .size:           8
        .value_kind:     global_buffer
      - .actual_access:  write_only
        .address_space:  global
        .offset:         96
        .size:           8
        .value_kind:     global_buffer
    .group_segment_fixed_size: 1024
    .kernarg_segment_align: 8
    .kernarg_segment_size: 104
    .language:       OpenCL C
    .language_version:
      - 2
      - 0
    .max_flat_workgroup_size: 512
    .name:           _Z4k_l1PK15HIP_vector_typeIiLj4EEPiPKfS5_S5_S5_S5_S5_S5_PDF16_PfS6_S6_
    .private_segment_fixed_size: 0
    .sgpr_count:     22
    .sgpr_spill_count: 0
    .symbol:         _Z4k_l1PK15HIP_vector_typeIiLj4EEPiPKfS5_S5_S5_S5_S5_S5_PDF16_PfS6_S6_.kd
    .uniform_work_group_size: 1
    .uses_dynamic_stack: false
    .vgpr_count:     24
    .vgpr_spill_count: 0
    .wavefront_size: 64
  - .agpr_count:     0
    .args:
      - .actual_access:  read_only
        .address_space:  global
        .offset:         0
        .size:           8
        .value_kind:     global_buffer
      - .actual_access:  read_only
        .address_space:  global
        .offset:         8
        .size:           8
        .value_kind:     global_buffer
      - .actual_access:  read_only
        .address_space:  global
        .offset:         16
        .size:           8
        .value_kind:     global_buffer
      - .actual_access:  write_only
        .address_space:  global
        .offset:         24
        .size:           8
        .value_kind:     global_buffer
      - .actual_access:  write_only
        .address_space:  global
        .offset:         32
        .size:           8
        .value_kind:     global_buffer
      - .actual_access:  read_only
        .address_space:  global
        .offset:         40
        .size:           8
        .value_kind:     global_buffer
      - .actual_access:  read_only
        .address_space:  global
        .offset:         48
        .size:           8
        .value_kind:     global_buffer
      - .actual_access:  read_only
        .address_space:  global
        .offset:         56
        .size:           8
        .value_kind:     global_buffer
      - .actual_access:  write_only
        .address_space:  global
        .offset:         64
        .size:           8
        .value_kind:     global_buffer
      - .actual_access:  write_only
        .address_space:  global
        .offset:         72
        .size:           8
        .value_kind:     global_buffer
    .group_segment_fixed_size: 53248
    .kernarg_segment_align: 8
    .kernarg_segment_size: 80
    .language:       OpenCL C
    .language_version:
      - 2
      - 0
    .max_flat_workgroup_size: 512
    .name:           _Z4k_l2PK15HIP_vector_typeIiLj4EES2_PKiPiS5_PKfPKDv8_DF16_S7_PDF16_SB_
    .private_segment_fixed_size: 0
    .sgpr_count:     34
    .sgpr_spill_count: 0
    .symbol:         _Z4k_l2PK15HIP_vector_typeIiLj4EES2_PKiPiS5_PKfPKDv8_DF16_S7_PDF16_SB_.kd
    .uniform_work_group_size: 1
    .uses_dynamic_stack: false
    .vgpr_count:     126
    .vgpr_spill_count: 0
    .wavefront_size: 64
